# down-proj weight conversion moved from in_proj phase into chunk-0 expert GEMM1 epilogues (1 unit per GEMM unit); attention 12 + top-k 5 units enumerate gate/up only; none left in phase 2
# baseline (speedup 1.0000x reference)
; #define LAS __attribute__((address_space(3)))
; __device__ __forceinline__ void convert_experts(Frame& F, int lo, int hi) {
;     const int gw = F.vcu * 8 + F.wave, NGW = F.G * 8;
;     LAS unsigned char* scr = F.lds + F.wave * 16384;
;     unsigned char* W1t = WSP(F, WS_W1T, unsigned char); unsigned char* W2t = WSP(F, WS_W2T, unsigned char);
;     const float* weg = F.a->in[I_WEG]; const float* weu = F.a->in[I_WEU]; const float* wed = F.a->in[I_WED];
;     const float* wsg = F.a->in[I_WSG]; const float* wsu = F.a->in[I_WSU]; const float* wsd = F.a->in[I_WSD];
;     ...
;     constexpr int NPAIRS = CONV_ITEMS / 2;
;     (void)lo; (void)hi;
;     ...
;     if (gw < NPAIRS) {
;         const int ns = 2 * ((NPAIRS - gw + NGW - 1) / NGW);
;         int sq = 0, r = CONV_RIDX(0);
;         TItem tc, tn; CONV_DESC(r, tc); tn = tc;
;         int p = 0; bool first = true;
;         titem_issue(tc, F.lane, scr);
;         for (;;) {
;             const bool more = sq + 1 < ns; const int rn = more ? CONV_RIDX(sq + 1) : r;
.Lcv1_vcu:
	s_lshl_b32 s11, s11, 3
	s_add_u32 s89, s11, s9
	s_lshl_b32 s71, s8, 3
	s_mul_i32 s10, s71, 25
	s_add_u32 s89, s89, s10
	s_mov_b32 s90, 49344
	s_mov_b32 s69, s89
	s_add_u32 s86, s84, 0x9180000
	s_addc_u32 s87, s85, 0
	s_add_u32 s84, s84, 0x1100000
	s_addc_u32 s85, s85, 0
	s_cmp_ge_u32 s89, s90
	s_cbranch_scc1 .Lcv1_done
	s_cmp_lt_u32 s69, s90
	s_cbranch_scc0 .Lcv1_dummyA1
	s_lshr_b32 s10, s69, 6
	s_and_b32 s12, s69, 63
	s_mul_hi_u32 s14, s10, 0xaaaaaaab
	s_lshr_b32 s14, s14, 1
	s_mul_i32 s11, s14, 3
	s_sub_u32 s11, s10, s11
	s_cmp_lt_u32 s14, 256
	s_cselect_b32 s10, s14, 0
	s_cselect_b64 s[44:45], -1, 0
	s_lshl_b32 s10, s10, 20
	s_cmp_eq_u32 s11, 2
	s_cbranch_scc1 .Lcv1_downA1
	s_cmp_eq_u32 s11, 0
	s_cselect_b64 s[4:5], s[72:73], s[74:75]
	s_cselect_b64 s[38:39], s[78:79], s[80:81]
	s_mov_b32 s94, 0xc3317218
	s_cselect_b32 s94, 0xc2b8aa3b, s94
	s_cmp_lg_u64 s[44:45], 0
	s_cselect_b64 s[4:5], s[4:5], s[38:39]
	s_lshr_b32 s38, s12, 3
	s_and_b32 s39, s12, 7
	s_lshl_b32 s8, s38, 17
	s_add_u32 s10, s10, s8
	s_lshl_b32 s8, s39, 7
	s_add_u32 s10, s10, s8
	s_add_u32 s4, s4, s10
	s_addc_u32 s5, s5, 0
	s_lshl_b32 s14, s14, 19
	s_lshr_b32 s8, s39, 2
	s_lshl_b32 s8, s8, 18
	s_add_u32 s14, s14, s8
	s_and_b32 s8, s39, 3
	s_lshl_b32 s8, s8, 15
	s_add_u32 s14, s14, s8
	s_lshl_b32 s8, s11, 17
	s_add_u32 s14, s14, s8
	s_lshl_b32 s8, s38, 7
	s_add_u32 s14, s14, s8
	s_add_u32 s92, s84, s14
	s_addc_u32 s93, s85, 0
	s_movk_i32 s25, 0x400
	s_movk_i32 s27, 0x1000
	s_movk_i32 s8, 0x400
	s_movk_i32 s9, 0x4000
	s_branch .Lcv1_goA1

; #define LAS __attribute__((address_space(3)))
; __device__ __forceinline__ void convert_experts(Frame& F, int lo, int hi) {
;     ...
;     constexpr int NPAIRS = CONV_ITEMS / 2;
;     (void)lo; (void)hi;
; __device__ __forceinline__ void phase_attn(Frame& F) {
;     ...
;         const unsigned qrow = __umul24((unsigned)(128 * cu.n + ql), (unsigned)cu.d);
;         const float c1 = 0.125f * LOG2E;
;         const float nc2 = -__builtin_amdgcn_exp2f(-(float)(cu.h + 1)) * (float)cu.d * LOG2E;
;         const bool first = cu.n == 0;
;         f32x4 St[9];
;         const f32x4 eb = (f32x4){ef[0], ef[1], ef[2], ef[3]} * nc2;
;         float mx = -INFINITY;
;         bf16x8 kf[9][2];
; #pragma unroll
;         for (int T = 0; T < 9; ++T) { LAS unsigned char* ka = kb + (16 * (w + T) + fr) * ATT_ROWB + fq * 16; kf[T][0] = *(LAS bf16x8*)ka; kf[T][1] = *(LAS bf16x8*)(ka + 64); }
.Lcq_wd:
	v_mov_b64_e32 v[48:49], v[4:5]
	v_mov_b64_e32 v[46:47], v[2:3]
	v_mov_b64_e32 v[44:45], v[8:9]
	v_mov_b64_e32 v[42:43], v[6:7]
	s_lshl_b32 s65, 1, s35
	s_waitcnt lgkmcnt(0)
	s_barrier
	s_add_i32 s37, s30, 1
	v_cvt_f32_u32_e32 v54, s37
	v_cvt_f32_u32_e32 v55, s65
	v_add_u32_e32 v110, s85, v82
	v_add_u32_e32 v58, v110, v90
	v_exp_f32_e64 v54, -v54
	v_add_u32_e32 v66, v110, v91
	v_add_u32_e32 v74, v110, v92
	v_add_u32_e32 v111, v110, v93
	v_mul_f32_e32 v79, v55, v54
	ds_read_b128 v[54:57], v58
	ds_read_b128 v[58:61], v58 offset:64
	ds_read_b128 v[62:65], v66
	ds_read_b128 v[66:69], v66 offset:64
	ds_read_b128 v[70:73], v74
	ds_read_b128 v[74:77], v74 offset:64
	ds_read_b128 v[112:115], v111
	ds_read_b128 v[116:119], v111 offset:64
	v_add_u32_e32 v111, v110, v94
	ds_read_b128 v[120:123], v111
	ds_read_b128 v[124:127], v111 offset:64
	v_add_u32_e32 v111, v110, v95
	ds_read_b128 v[128:131], v111
	ds_read_b128 v[132:135], v111 offset:64
	v_add_u32_e32 v111, v110, v96
	ds_read_b128 v[136:139], v111
	ds_read_b128 v[140:143], v111 offset:64
	v_add_u32_e32 v111, v110, v97
	v_add_u32_e32 v110, v110, v98
	ds_read_b128 v[144:147], v111
	ds_read_b128 v[148:151], v111 offset:64
	ds_read_b128 v[152:155], v110
	ds_read_b128 v[156:159], v110 offset:64
	s_sub_u32 s32, s32, 1
	s_cmp_lt_i32 s32, 0
	s_cbranch_scc0 .Lcq_cont_l
	s_mov_b32 s32, 3
	s_mov_b32 s95, 0
	s_cmp_eq_u32 s90, 0
	s_cbranch_scc1 .Lcq_none_l
	s_sub_u32 s90, s90, 1
	s_lshr_b32 s98, s89, 6
	s_and_b32 s99, s89, 63
	s_lshr_b32 s100, s98, 1
	s_and_b32 s101, s98, 1
	s_cmp_lt_u32 s100, 256
	s_cselect_b32 s98, 0, 3
	s_cselect_b32 s95, s100, 0
	s_add_u32 s98, s98, s101
	s_lshl_b32 s98, s98, 1
	v_readlane_b32 s96, v253, s98
	s_add_u32 s98, s98, 1
	v_readlane_b32 s97, v253, s98
	s_lshl_b32 s95, s95, 20
	s_nop 3
	s_add_u32 s96, s96, s95
	s_addc_u32 s97, s97, 0
	s_cmp_eq_u32 s101, 2
	s_cbranch_scc1 .Lcq_down_l
	s_lshr_b32 s95, s99, 3
	s_and_b32 s99, s99, 7
	s_lshl_b32 s98, s95, 17
	s_add_u32 s96, s96, s98
	s_addc_u32 s97, s97, 0
	s_lshl_b32 s98, s99, 7
	s_add_u32 s96, s96, s98
	s_addc_u32 s97, s97, 0
	s_lshl_b32 s100, s100, 19
	s_lshr_b32 s98, s99, 2
	s_lshl_b32 s98, s98, 18
	s_add_u32 s100, s100, s98
	s_and_b32 s98, s99, 3
	s_lshl_b32 s98, s98, 15
	s_add_u32 s100, s100, s98
	s_lshl_b32 s98, s101, 17
	s_add_u32 s100, s100, s98
	s_lshl_b32 s98, s95, 7
	s_add_u32 s100, s100, s98
	v_readlane_b32 s92, v253, 12
	v_readlane_b32 s93, v253, 13
	s_mov_b32 s94, 0xc3317218
	s_cmp_eq_u32 s101, 0
	s_cselect_b32 s94, 0xc2b8aa3b, s94
	s_nop 3
	s_add_u32 s92, s92, s100
	s_addc_u32 s93, s93, 0
	s_movk_i32 s95, 0x400
	s_movk_i32 s98, 0x400
	s_branch .Lcq_go_l

; __device__ __forceinline__ void convert_experts(Frame& F, int lo, int hi) {
;     ...
;     constexpr int NPAIRS = CONV_ITEMS / 2;
;     (void)lo; (void)hi;
.Lcq_tail:
	s_sub_u32 s32, s32, 1
	s_cmp_lt_i32 s32, 0
	s_cbranch_scc0 .Lcq_cont_t
	s_mov_b32 s32, 3
	s_mov_b32 s95, 0
	s_cmp_eq_u32 s90, 0
	s_cbranch_scc1 .Lcq_none_t
	s_sub_u32 s90, s90, 1
	s_lshr_b32 s98, s89, 6
	s_and_b32 s99, s89, 63
	s_lshr_b32 s100, s98, 1
	s_and_b32 s101, s98, 1
	s_cmp_lt_u32 s100, 256
	s_cselect_b32 s98, 0, 3
	s_cselect_b32 s95, s100, 0
	s_add_u32 s98, s98, s101
	s_lshl_b32 s98, s98, 1
	v_readlane_b32 s96, v253, s98
	s_add_u32 s98, s98, 1
	v_readlane_b32 s97, v253, s98
	s_lshl_b32 s95, s95, 20
	s_nop 3
	s_add_u32 s96, s96, s95
	s_addc_u32 s97, s97, 0
	s_cmp_eq_u32 s101, 2
	s_cbranch_scc1 .Lcq_down_t
	s_lshr_b32 s95, s99, 3
	s_and_b32 s99, s99, 7
	s_lshl_b32 s98, s95, 17
	s_add_u32 s96, s96, s98
	s_addc_u32 s97, s97, 0
	s_lshl_b32 s98, s99, 7
	s_add_u32 s96, s96, s98
	s_addc_u32 s97, s97, 0
	s_lshl_b32 s100, s100, 19
	s_lshr_b32 s98, s99, 2
	s_lshl_b32 s98, s98, 18
	s_add_u32 s100, s100, s98
	s_and_b32 s98, s99, 3
	s_lshl_b32 s98, s98, 15
	s_add_u32 s100, s100, s98
	s_lshl_b32 s98, s101, 17
	s_add_u32 s100, s100, s98
	s_lshl_b32 s98, s95, 7
	s_add_u32 s100, s100, s98
	v_readlane_b32 s92, v253, 12
	v_readlane_b32 s93, v253, 13
	s_mov_b32 s94, 0xc3317218
	s_cmp_eq_u32 s101, 0
	s_cselect_b32 s94, 0xc2b8aa3b, s94
	s_nop 3
	s_add_u32 s92, s92, s100
	s_addc_u32 s93, s93, 0
	s_movk_i32 s95, 0x400
	s_movk_i32 s98, 0x400
	s_branch .Lcq_go_t

; #define LAS __attribute__((address_space(3)))
; __device__ __forceinline__ void router_topk(Frame& F, int tile) {
;     const float* logits = WSP(F, WS_B, float); const float* br = F.a->in[I_BR];
;     int* tk_e = WSP(F, WS_TOPK_E, int); float* tk_g = WSP(F, WS_TOPK_G, float); int* tk_p = WSP(F, WS_TOPK_P, int);
;     int* gcnt = (int*)(F.a->ws + WS_CTL + CTL_CNT);
;     LAS int* hist = (LAS int*)F.lds; LAS int* base = hist + 256;
;     const int lane = F.lane, w = F.wave;
;     if (F.tid < 256) hist[F.tid] = 0;
;     __syncthreads();
;     const f32x4 bias = *(const f32x4*)(br + 4 * lane);
;     f32x4 lgn = *(const f32x4*)(logits + (size_t)(tile * 256 + w * 32) * 256 + 4 * lane);
;     int pe = 0, pp = 0; float pg = 0.f;
;     int* dumpi = (int*)(F.a->ws + WS_B + ((size_t)128 << 20));
.Lcvt_vcu:
	s_add_u32 s69, s41, s40
	s_and_b32 s69, s69, 3
	s_lshl_b32 s41, s41, 3
	s_add_u32 s89, s41, s40
	s_lshl_b32 s71, s64, 3
	s_mul_i32 s39, s71, 12
	s_add_u32 s89, s89, s39
	s_movk_i32 s90, 5
	s_mov_b32 s32, 0
	s_add_u32 s86, s84, 0x9180000
	s_addc_u32 s87, s85, 0
	s_add_u32 s84, s84, 0x1100000
	s_addc_u32 s85, s85, 0
	s_add_u32 s14, s8, 0x900000
	s_addc_u32 s15, s9, 0
	s_add_u32 s16, s8, 0xb00000
	s_addc_u32 s17, s9, 0
	s_add_u32 s18, s8, 0xd00000
	s_addc_u32 s19, s9, 0
	v_mov_b32_e32 v131, 0
	s_add_u32 s20, s8, 0x4000
	v_mov_b32_e32 v133, v131
	s_addc_u32 s21, s9, 0
	v_lshl_add_u64 v[2:3], s[8:9], 0, v[132:133]
	s_mov_b64 s[8:9], 0x1d1c0000
	s_waitcnt vmcnt(0)
	v_lshl_add_u64 v[12:13], v[2:3], 0, s[8:9]
	s_mov_b64 s[8:9], 0x1d1c0100
	s_movk_i32 s4, 0x100
	v_mov_b32_e32 v135, v131
	v_lshl_add_u64 v[14:15], v[2:3], 0, s[8:9]
	s_mov_b64 s[8:9], 0x1d1c0200
	v_cmp_gt_i32_e64 s[4:5], s4, v1
	s_mov_b32 s26, 0
	v_lshl_add_u32 v22, v1, 2, 0
	s_lshl_b32 s27, s49, 5
	v_lshl_add_u64 v[10:11], s[6:7], 0, v[134:135]
	v_cmp_gt_u32_e64 s[6:7], 8, v130
	v_lshl_add_u64 v[16:17], v[2:3], 0, s[8:9]
	v_mov_b64_e32 v[18:19], 0x100
	v_mov_b64_e32 v[20:21], 0xff
	v_mov_b32_e32 v23, 0xff800000
	v_mov_b32_e32 v24, 1
	s_waitcnt vmcnt(0)
	s_barrier
	s_branch .LBB0_532

; __device__ __forceinline__ float fast_exp2(float x) { return __builtin_amdgcn_exp2f(x); }
; __device__ __forceinline__ float fast_rcp(float x) { return __builtin_amdgcn_rcpf(x); }
; __device__ __forceinline__ void convert_experts(Frame& F, int lo, int hi) {
;     ...
;     constexpr int NPAIRS = CONV_ITEMS / 2;
;     (void)lo; (void)hi;
; __device__ __forceinline__ void router_topk(Frame& F, int tile) {
;     ...
;     for (int i = 0; i < 32; ++i) {
;         const int tok = tile * 256 + w * 32 + i;
;         const f32x4 lg = lgn;
;         {
;           const bool real = lane < 8 && i > 0; const size_t o = (size_t)(tok - 1) * 8 + lane;
;           int* de = real ? tk_e + o : dumpi + lane; float* dg = real ? tk_g + o : (float*)dumpi + 64 + lane; int* dp = real ? tk_p + o : dumpi + 128 + lane;
;           *de = pe; *dg = pg; *dp = pp; }
;         lgn = *(const f32x4*)(logits + (size_t)(i + 1 < 32 ? tok + 1 : tok) * 256 + 4 * lane);
;         float sc[4], ch[4];
; #pragma unroll
;         for (int j = 0; j < 4; ++j) { sc[j] = fast_rcp(1.f + fast_exp2(-lg[j] * LOG2E)); ch[j] = sc[j] + bias[j]; }
.Lcvt_wd:
	v_mov_b64_e32 v[30:31], v[8:9]
	s_cmp_lg_u32 s24, 31
	v_mov_b64_e32 v[28:29], v[6:7]
	v_lshl_add_u64 v[6:7], s[30:31], 0, v[130:131]
	s_cselect_b64 s[30:31], -1, 0
	v_lshlrev_b64 v[6:7], 2, v[6:7]
	s_cmp_lg_u64 s[30:31], 0
	v_lshl_add_u64 v[8:9], s[14:15], 0, v[6:7]
	v_lshl_add_u64 v[32:33], s[16:17], 0, v[6:7]
	v_lshl_add_u64 v[6:7], s[18:19], 0, v[6:7]
	s_addc_u32 s8, s8, 0
	v_cndmask_b32_e32 v9, v13, v9, vcc
	v_cndmask_b32_e32 v8, v12, v8, vcc
	v_cndmask_b32_e32 v6, v16, v6, vcc
	s_ashr_i32 s9, s8, 31
	v_cndmask_b32_e32 v33, v15, v33, vcc
	v_cndmask_b32_e32 v32, v14, v32, vcc
	v_cndmask_b32_e32 v7, v17, v7, vcc
	global_store_dword v[8:9], v27, off
	global_store_dword v[32:33], v26, off
	s_waitcnt lgkmcnt(0)
	global_store_dword v[6:7], v25, off
	v_mul_f32_e32 v6, 0xbfb8aa3b, v28
	s_lshl_b64 s[8:9], s[8:9], 10
	v_exp_f32_e32 v28, v6
	v_lshl_add_u64 v[6:7], v[10:11], 0, s[8:9]
	global_load_dwordx4 v[6:9], v[6:7], off
	s_sub_u32 s69, s69, 1
	s_cmp_lt_i32 s69, 0
	s_cbranch_scc0 .Lcvt_none_l
	s_mov_b32 s69, 3
	s_cmp_eq_u32 s90, 0
	s_cbranch_scc1 .Lcvt_none_l
	s_cmp_lg_u32 s32, 0
	s_cbranch_scc1 .Lcvt_none_l
	s_cmp_lt_u32 s89, 32896
	s_cbranch_scc1 .Lcvt_ok_l
	s_mov_b32 s90, 0
	s_branch .Lcvt_none_l
.Lcvt_ok_l:
	s_sub_u32 s90, s90, 1
	s_lshr_b32 s39, s89, 6
	s_and_b32 s40, s89, 63
	s_lshr_b32 s42, s39, 1
	s_and_b32 s41, s39, 1
	s_cmp_lt_u32 s42, 256
	s_cselect_b32 s100, s42, 0
	s_cselect_b64 s[44:45], -1, 0
	s_lshl_b32 s100, s100, 20
	s_cmp_eq_u32 s41, 2
	s_cbranch_scc1 .Lcvt_down_l
	s_cmp_eq_u32 s41, 0
	s_cselect_b64 s[96:97], s[72:73], s[74:75]
	s_cselect_b64 s[98:99], s[78:79], s[80:81]
	s_mov_b32 s94, 0xc3317218
	s_cselect_b32 s94, 0xc2b8aa3b, s94
	s_cmp_lg_u64 s[44:45], 0
	s_cselect_b64 s[96:97], s[96:97], s[98:99]
	s_lshr_b32 s55, s40, 3
	s_and_b32 s58, s40, 7
	s_lshl_b32 s39, s55, 17
	s_add_u32 s100, s100, s39
	s_lshl_b32 s39, s58, 7
	s_add_u32 s100, s100, s39
	s_add_u32 s96, s96, s100
	s_addc_u32 s97, s97, 0
	s_lshl_b32 s42, s42, 19
	s_lshr_b32 s39, s58, 2
	s_lshl_b32 s39, s39, 18
	s_add_u32 s42, s42, s39
	s_and_b32 s39, s58, 3
	s_lshl_b32 s39, s39, 15
	s_add_u32 s42, s42, s39
	s_lshl_b32 s39, s41, 17
	s_add_u32 s42, s42, s39
	s_lshl_b32 s39, s55, 7
	s_add_u32 s42, s42, s39
	s_add_u32 s92, s84, s42
	s_addc_u32 s93, s85, 0
	s_movk_i32 s36, 0x400
	s_movk_i32 s38, 0x1000
	s_movk_i32 s98, 0x400
	s_branch .Lcvt_go_l

; __device__ __forceinline__ void convert_experts(Frame& F, int lo, int hi) {
;     ...
;     constexpr int NPAIRS = CONV_ITEMS / 2;
;     (void)lo; (void)hi;
.LBB0_552:
.Lcvt_catch:
	s_cmp_eq_u32 s90, 0
	s_cbranch_scc1 .Lcvt_catch_done
	s_cmp_lt_u32 s89, 32896
	s_cbranch_scc0 .Lcvt_catch_done
	s_sub_u32 s90, s90, 1
	s_lshr_b32 s39, s89, 6
	s_and_b32 s40, s89, 63
	s_lshr_b32 s42, s39, 1
	s_and_b32 s41, s39, 1
	s_cmp_lt_u32 s42, 256
	s_cselect_b32 s100, s42, 0
	s_cselect_b64 s[44:45], -1, 0
	s_lshl_b32 s100, s100, 20
	s_cmp_eq_u32 s41, 2
	s_cbranch_scc1 .Lcvt_down_c
	s_cmp_eq_u32 s41, 0
	s_cselect_b64 s[96:97], s[72:73], s[74:75]
	s_cselect_b64 s[98:99], s[78:79], s[80:81]
	s_mov_b32 s94, 0xc3317218
	s_cselect_b32 s94, 0xc2b8aa3b, s94
	s_cmp_lg_u64 s[44:45], 0
	s_cselect_b64 s[96:97], s[96:97], s[98:99]
	s_lshr_b32 s55, s40, 3
	s_and_b32 s58, s40, 7
	s_lshl_b32 s39, s55, 17
	s_add_u32 s100, s100, s39
	s_lshl_b32 s39, s58, 7
	s_add_u32 s100, s100, s39
	s_add_u32 s96, s96, s100
	s_addc_u32 s97, s97, 0
	s_lshl_b32 s42, s42, 19
	s_lshr_b32 s39, s58, 2
	s_lshl_b32 s39, s39, 18
	s_add_u32 s42, s42, s39
	s_and_b32 s39, s58, 3
	s_lshl_b32 s39, s39, 15
	s_add_u32 s42, s42, s39
	s_lshl_b32 s39, s41, 17
	s_add_u32 s42, s42, s39
	s_lshl_b32 s39, s55, 7
	s_add_u32 s42, s42, s39
	s_add_u32 s92, s84, s42
	s_addc_u32 s93, s85, 0
	s_movk_i32 s36, 0x400
	s_movk_i32 s38, 0x1000
	s_movk_i32 s98, 0x400
	s_branch .Lcvt_go_c

; #define LAS __attribute__((address_space(3)))
; #define CAS __attribute__((address_space(4)))
;     __device__ __forceinline__ void init(LAS unsigned char* lds_, const void* A_, const void* W_, const int* rowtok, const TileTabs& T, int chunk, int tid_) {
;         lds = lds_; tid = tid_; A = (const char*)A_; W = (const char*)W_;
;         const int U = T.ntiles * NTN, x8 = blockIdx.x & 7, r8 = blockIdx.x >> 3, G8 = gridDim.x >> 3;
;         const int q = (((U + 7) >> 3) + NTN - 1) / NTN * NTN;
;         const int lo = x8 * q + r8, hi = (x8 + 1) * q < U ? (x8 + 1) * q : U;
;         int cnt = hi > lo ? (hi - lo + G8 - 1) / G8 : 0; cnt = cnt > (G1 ? UT_MAXU : 64) ? (G1 ? UT_MAXU : 64) : cnt;
;         n = cnt;
; __device__ __forceinline__ Frame make_frame(LAS unsigned char* lds) {
;     Frame F; F.lds = lds;
;     int t = threadIdx.x; asm volatile("" : "+v"(t));
;     F.tid = t; F.lane = t & 63; F.wave = __builtin_amdgcn_readfirstlane(t >> 6);
;     const CAS Args* a = (const CAS Args*)__builtin_amdgcn_kernarg_segment_ptr(); asm volatile("" : "+s"(a)); F.a = a;
;     F.G = gridDim.x; { const int bx = blockIdx.x; F.vcu = (F.G % 8 == 0) ? (bx % 8) * (F.G / 8) + bx / 8 : bx; }
;     return F;
.LBB0_703:
	s_add_u32 s64, s0, 0xd0
	s_addc_u32 s65, s1, 0
	s_and_b32 s3, s2, 7
	s_lshr_b32 s33, s2, 3
	s_cmp_lt_i32 s62, 10
	s_cselect_b64 s[4:5], -1, 0
	s_cmp_gt_i32 s63, 9
	s_cselect_b64 s[6:7], -1, 0
	s_and_b64 s[38:39], s[4:5], s[6:7]
	s_andn2_b64 vcc, exec, s[38:39]
	s_cbranch_vccnz .LBB0_761
	v_mov_b32_e32 v7, v0
	s_load_dwordx2 s[78:79], s[0:1], 0x90
	s_load_dwordx2 s[80:81], s[0:1], 0xa8
	s_load_dwordx2 s[82:83], s[0:1], 0xc0
	s_load_dword s84, s[0:1], 0xd0
	v_and_b32_e32 v253, 63, v0
	v_and_b32_e32 v254, 7, v253
	v_lshlrev_b32_e32 v254, 4, v254
	v_lshrrev_b32_e32 v253, 3, v253
	v_readfirstlane_b32 s85, v0
	s_waitcnt lgkmcnt(0)
	s_lshr_b32 s85, s85, 6
	s_and_b32 s86, s84, 7
	s_mov_b32 s87, s2
	s_cmp_lg_u32 s86, 0
	s_cbranch_scc1 .Lg1c_vcu
	s_and_b32 s86, s2, 7
	s_lshr_b32 s87, s84, 3
	s_mul_i32 s87, s87, s86
	s_lshr_b32 s86, s2, 3
	s_add_u32 s87, s87, s86
.Lg1c_vcu:
	s_lshl_b32 s87, s87, 3
	s_add_u32 s89, s87, s85
	s_lshl_b32 s90, s84, 3
	s_add_u32 s82, s82, 0x9180000
	s_addc_u32 s83, s83, 0
	s_mov_b32 s32, 0
	s_mov_b32 s94, 0x42800000
	s_mov_b32 s95, s94
	s_mov_b64 s[4:5], s[0:1]
	s_load_dwordx2 s[24:25], s[4:5], 0xc0
	v_mov_b32_e32 v1, 0x98000
	s_load_dword s4, s[64:65], 0x0
	s_waitcnt lgkmcnt(0)
	s_mov_b32 s36, 0
	global_load_dword v1, v1, s[24:25] offset:1024
	s_lshr_b32 s6, s4, 3
	s_waitcnt vmcnt(0)
	v_readfirstlane_b32 s4, v1
	s_lshl_b32 s4, s4, 1
	s_add_i32 s5, s4, 7
	s_ashr_i32 s5, s5, 3
	s_add_i32 s5, s5, 1
	s_lshr_b32 s7, s5, 31
	s_add_i32 s5, s5, s7
	s_and_b32 s5, s5, -2
	s_mul_i32 s8, s5, s3
	s_add_i32 s7, s8, s33
	s_add_i32 s8, s8, s5
	s_min_i32 s4, s8, s4
	s_cmp_le_i32 s4, s7
	s_cbranch_scc1 .LBB0_706
	v_cvt_f32_u32_e32 v1, s6
	s_not_b32 s5, s7
	s_sub_i32 s8, 0, s6
	s_add_i32 s5, s6, s5
	v_rcp_iflag_f32_e32 v1, v1
	s_add_i32 s5, s5, s4
	s_ashr_i32 s4, s5, 31
	s_abs_i32 s5, s5
	v_mul_f32_e32 v1, 0x4f7ffffe, v1
	v_cvt_u32_f32_e32 v1, v1
	s_nop 0
	v_readfirstlane_b32 s9, v1
	s_mul_i32 s8, s8, s9
	s_mul_hi_u32 s8, s9, s8
	s_add_i32 s9, s9, s8
	s_mul_hi_u32 s8, s5, s9
	s_mul_i32 s9, s8, s6
	s_sub_i32 s5, s5, s9
	s_add_i32 s10, s8, 1
	s_sub_i32 s9, s5, s6
	s_cmp_ge_u32 s5, s6
	s_cselect_b32 s8, s10, s8
	s_cselect_b32 s5, s9, s5
	s_add_i32 s9, s8, 1
	s_cmp_ge_u32 s5, s6
	s_cselect_b32 s5, s9, s8
	s_xor_b32 s5, s5, s4
	s_sub_i32 s4, s5, s4
	s_min_i32 s36, s4, 20

; #define PG8_BAR __builtin_amdgcn_s_barrier()
;     ...
;         if constexpr (ALIGN_EPI) { if (wr == 0) PG8_BAR; }
;         if constexpr (Epi::F8) asm volatile("s_nop 15\n\ts_nop 15" ::: "memory");
;         if (!(probe & 2)) E(acc, cur, wr, wc, fr, fq);
;         if (!has_next) break;
.LBB0_728:
	s_cmp_eq_u32 s32, 0
	s_cbranch_scc1 .Lg1c_p_none
	s_cmp_eq_u32 s43, 0x100
	s_cbranch_scc0 .Lg1c_p_w0
	s_waitcnt vmcnt(8)
	s_branch .Lg1c_p_go

; #define LAS __attribute__((address_space(3)))
; __device__ __forceinline__ void titem_finish(const TItem& t, int lane, const LAS unsigned char* buf) {
;     const int nblk = t.N / 32, kb = t.item / nblk, nb = t.item % nblk, k0 = 64 * kb, n0 = 32 * nb;
;     const int d0 = t.gmode == 0 ? n0 : ((n0 >> 7) * 256 + (n0 & 127) + (t.gmode == 2 ? 128 : 0));
;     const int c = lane & 7;
;     const LAS float* sb = (const LAS float*)buf;
;     float v[4][8];
;     const float wsc = t.scale;
; #pragma unroll
;     for (int j = 0; j < 4; ++j) { const int n = (lane >> 3) + 8 * j; const LAS float* s = sb + (8 * c) * 32 + 4 * ((n >> 2) ^ c) + (n & 3);
; #pragma unroll
;         for (int q = 0; q < 8; ++q) v[j][q] = s[32 * q] * wsc; }
;     if (t.f8) {
; #pragma unroll
;         for (int j = 0; j < 4; ++j) { const int n = (lane >> 3) + 8 * j;
;             int w0 = __builtin_amdgcn_cvt_pk_fp8_f32(v[j][0], v[j][1], 0, false); w0 = __builtin_amdgcn_cvt_pk_fp8_f32(v[j][2], v[j][3], w0, true);
;             int w1 = __builtin_amdgcn_cvt_pk_fp8_f32(v[j][4], v[j][5], 0, false); w1 = __builtin_amdgcn_cvt_pk_fp8_f32(v[j][6], v[j][7], w1, true);
;             u32x2 o; o.x = (unsigned)w0; o.y = (unsigned)w1;
;             __builtin_nontemporal_store(o, (u32x2*)((unsigned char*)t.WT + (size_t)(d0 + n) * t.K + k0 + 8 * c)); }
.Lg1c_p_go:
	v_pk_mul_f32 v[16:17], v[16:17], s[94:95]
	v_pk_mul_f32 v[18:19], v[18:19], s[94:95]
	v_pk_mul_f32 v[20:21], v[20:21], s[94:95]
	v_pk_mul_f32 v[22:23], v[22:23], s[94:95]
	v_pk_mul_f32 v[24:25], v[24:25], s[94:95]
	v_pk_mul_f32 v[26:27], v[26:27], s[94:95]
	v_pk_mul_f32 v[28:29], v[28:29], s[94:95]
	v_pk_mul_f32 v[30:31], v[30:31], s[94:95]
	v_pk_mul_f32 v[32:33], v[32:33], s[94:95]
	v_pk_mul_f32 v[34:35], v[34:35], s[94:95]
	v_pk_mul_f32 v[36:37], v[36:37], s[94:95]
	v_pk_mul_f32 v[38:39], v[38:39], s[94:95]
	v_pk_mul_f32 v[40:41], v[40:41], s[94:95]
	v_pk_mul_f32 v[42:43], v[42:43], s[94:95]
	v_pk_mul_f32 v[44:45], v[44:45], s[94:95]
	v_pk_mul_f32 v[46:47], v[46:47], s[94:95]
	v_pk_mul_f32 v[48:49], v[48:49], s[94:95]
	v_pk_mul_f32 v[50:51], v[50:51], s[94:95]
	v_pk_mul_f32 v[52:53], v[52:53], s[94:95]
	v_pk_mul_f32 v[54:55], v[54:55], s[94:95]
	v_pk_mul_f32 v[56:57], v[56:57], s[94:95]
	v_pk_mul_f32 v[58:59], v[58:59], s[94:95]
	v_pk_mul_f32 v[60:61], v[60:61], s[94:95]
	v_pk_mul_f32 v[62:63], v[62:63], s[94:95]
	v_pk_mul_f32 v[208:209], v[208:209], s[94:95]
	v_pk_mul_f32 v[210:211], v[210:211], s[94:95]
	v_pk_mul_f32 v[212:213], v[212:213], s[94:95]
	v_pk_mul_f32 v[214:215], v[214:215], s[94:95]
	v_pk_mul_f32 v[244:245], v[244:245], s[94:95]
	v_pk_mul_f32 v[246:247], v[246:247], s[94:95]
	v_pk_mul_f32 v[248:249], v[248:249], s[94:95]
	v_pk_mul_f32 v[250:251], v[250:251], s[94:95]
	s_movk_i32 s99, 0x40
	v_lshlrev_b32_e32 v255, 4, v253
	v_cvt_pk_fp8_f32 v2, v16, v20
	v_cvt_pk_fp8_f32 v3, v32, v36
	v_cvt_pk_fp8_f32 v4, v48, v52
	v_cvt_pk_fp8_f32 v5, v208, v212
	v_cvt_pk_fp8_f32 v6, v17, v21
	v_cvt_pk_fp8_f32 v7, v33, v37
	v_cvt_pk_fp8_f32 v8, v49, v53
	v_cvt_pk_fp8_f32 v9, v209, v213
	v_cvt_pk_fp8_f32 v10, v18, v22
	v_cvt_pk_fp8_f32 v11, v34, v38
	v_cvt_pk_fp8_f32 v12, v50, v54
	v_cvt_pk_fp8_f32 v13, v210, v214
	v_cvt_pk_fp8_f32 v72, v19, v23
	v_cvt_pk_fp8_f32 v73, v35, v39
	v_cvt_pk_fp8_f32 v74, v51, v55
	v_cvt_pk_fp8_f32 v75, v211, v215
	v_mad_u32_u24 v255, v254, s99, v255
	v_add_u32_e32 v241, 0x100, v255
	v_cvt_pk_fp8_f32 v2, v24, v28 op_sel:[0,0,1]
	v_cvt_pk_fp8_f32 v3, v40, v44 op_sel:[0,0,1]
	v_cvt_pk_fp8_f32 v4, v56, v60 op_sel:[0,0,1]
	v_cvt_pk_fp8_f32 v5, v244, v248 op_sel:[0,0,1]
	v_cvt_pk_fp8_f32 v6, v25, v29 op_sel:[0,0,1]
	v_cvt_pk_fp8_f32 v7, v41, v45 op_sel:[0,0,1]
	v_cvt_pk_fp8_f32 v8, v57, v61 op_sel:[0,0,1]
	v_cvt_pk_fp8_f32 v9, v245, v249 op_sel:[0,0,1]
	v_cvt_pk_fp8_f32 v10, v26, v30 op_sel:[0,0,1]
	v_cvt_pk_fp8_f32 v11, v42, v46 op_sel:[0,0,1]
	v_cvt_pk_fp8_f32 v12, v58, v62 op_sel:[0,0,1]
	v_cvt_pk_fp8_f32 v13, v246, v250 op_sel:[0,0,1]
	v_cvt_pk_fp8_f32 v72, v27, v31 op_sel:[0,0,1]
	v_cvt_pk_fp8_f32 v73, v43, v47 op_sel:[0,0,1]
	v_cvt_pk_fp8_f32 v74, v59, v63 op_sel:[0,0,1]
	v_cvt_pk_fp8_f32 v75, v247, v251 op_sel:[0,0,1]
	global_store_dwordx4 v255, v[2:5], s[92:93] nt
	global_store_dwordx4 v241, v[6:9], s[92:93] nt
	v_add_u32_e32 v255, 0x200, v255
	v_add_u32_e32 v241, 0x200, v241
	global_store_dwordx4 v255, v[10:13], s[92:93] nt
	global_store_dwordx4 v241, v[72:75], s[92:93] nt
	s_mov_b32 s32, 0

; #define LAS __attribute__((address_space(3)))
; __device__ __forceinline__ void titem_issue(const TItem& t, int lane, LAS unsigned char* buf) {
;     const int nblk = t.N / 32, kb = t.item / nblk, nb = t.item % nblk, k0 = 64 * kb, n0 = 32 * nb;
; #pragma unroll
;     for (int j = 0; j < 8; ++j) { const float* g = t.W + (size_t)(k0 + 8 * j + (lane >> 3)) * t.N + n0 + 4 * ((lane & 7) ^ j);
;         __builtin_amdgcn_global_load_lds((const unsigned*)g, (LAS unsigned*)(buf + j * 1024), 16, 0, 2); }
; }
.LBB0_741:
	s_cmp_lt_u32 s89, 16448
	s_cbranch_scc0 .Lg1c_none_l
	s_lshr_b32 s98, s89, 6
	s_and_b32 s99, s89, 63
	s_cmp_lt_u32 s98, 256
	s_cselect_b32 s100, s98, 0
	s_cselect_b64 s[96:97], s[78:79], s[80:81]
	s_lshl_b32 s100, s100, 20
	s_lshr_b32 s101, s99, 5
	s_and_b32 s99, s99, 31
	s_lshl_b32 s77, s101, 19
	s_add_u32 s100, s100, s77
	s_lshl_b32 s77, s99, 7
	s_add_u32 s100, s100, s77
	s_add_u32 s96, s96, s100
	s_addc_u32 s97, s97, 0
	s_lshl_b32 s98, s98, 18
	s_lshl_b32 s77, s99, 13
	s_add_u32 s98, s98, s77
	s_lshl_b32 s77, s101, 7
	s_add_u32 s98, s98, s77
	s_add_u32 s92, s82, s98
	s_addc_u32 s93, s83, 0
	v_lshl_add_u32 v255, v253, 16, v254
	global_load_dwordx4 v[16:19], v255, s[96:97] nt
	s_add_u32 s96, s96, 0x1000
	s_addc_u32 s97, s97, 0
	global_load_dwordx4 v[20:23], v255, s[96:97] nt
	s_add_u32 s96, s96, 0x1000
	s_addc_u32 s97, s97, 0
	global_load_dwordx4 v[24:27], v255, s[96:97] nt
	s_add_u32 s96, s96, 0x1000
	s_addc_u32 s97, s97, 0
	global_load_dwordx4 v[28:31], v255, s[96:97] nt
	s_add_u32 s96, s96, 0x1000
	s_addc_u32 s97, s97, 0
	global_load_dwordx4 v[32:35], v255, s[96:97] nt
	s_add_u32 s96, s96, 0x1000
	s_addc_u32 s97, s97, 0
	global_load_dwordx4 v[36:39], v255, s[96:97] nt
	s_add_u32 s96, s96, 0x1000
	s_addc_u32 s97, s97, 0
	global_load_dwordx4 v[40:43], v255, s[96:97] nt
	s_add_u32 s96, s96, 0x1000
	s_addc_u32 s97, s97, 0
	global_load_dwordx4 v[44:47], v255, s[96:97] nt
	s_add_u32 s96, s96, 0x1000
	s_addc_u32 s97, s97, 0
	global_load_dwordx4 v[48:51], v255, s[96:97] nt
	s_add_u32 s96, s96, 0x1000
	s_addc_u32 s97, s97, 0
	global_load_dwordx4 v[52:55], v255, s[96:97] nt
	s_add_u32 s96, s96, 0x1000
	s_addc_u32 s97, s97, 0
	global_load_dwordx4 v[56:59], v255, s[96:97] nt
	s_add_u32 s96, s96, 0x1000
	s_addc_u32 s97, s97, 0
	global_load_dwordx4 v[60:63], v255, s[96:97] nt
	s_add_u32 s96, s96, 0x1000
	s_addc_u32 s97, s97, 0
	global_load_dwordx4 v[208:211], v255, s[96:97] nt
	s_add_u32 s96, s96, 0x1000
	s_addc_u32 s97, s97, 0
	global_load_dwordx4 v[212:215], v255, s[96:97] nt
	s_add_u32 s96, s96, 0x1000
	s_addc_u32 s97, s97, 0
	global_load_dwordx4 v[244:247], v255, s[96:97] nt
	s_add_u32 s96, s96, 0x1000
	s_addc_u32 s97, s97, 0
	global_load_dwordx4 v[248:251], v255, s[96:97] nt
	s_add_u32 s89, s89, s90
	s_mov_b32 s32, 1

; #define LAS __attribute__((address_space(3)))
; __device__ __forceinline__ void titem_issue(const TItem& t, int lane, LAS unsigned char* buf) {
;     const int nblk = t.N / 32, kb = t.item / nblk, nb = t.item % nblk, k0 = 64 * kb, n0 = 32 * nb;
; #pragma unroll
;     for (int j = 0; j < 8; ++j) { const float* g = t.W + (size_t)(k0 + 8 * j + (lane >> 3)) * t.N + n0 + 4 * ((lane & 7) ^ j);
;         __builtin_amdgcn_global_load_lds((const unsigned*)g, (LAS unsigned*)(buf + j * 1024), 16, 0, 2); }
; }
; __device__ __forceinline__ void titem_finish(const TItem& t, int lane, const LAS unsigned char* buf) {
;     const int nblk = t.N / 32, kb = t.item / nblk, nb = t.item % nblk, k0 = 64 * kb, n0 = 32 * nb;
;     const int d0 = t.gmode == 0 ? n0 : ((n0 >> 7) * 256 + (n0 & 127) + (t.gmode == 2 ? 128 : 0));
;     const int c = lane & 7;
;     const LAS float* sb = (const LAS float*)buf;
;     float v[4][8];
;     const float wsc = t.scale;
; #pragma unroll
;     for (int j = 0; j < 4; ++j) { const int n = (lane >> 3) + 8 * j; const LAS float* s = sb + (8 * c) * 32 + 4 * ((n >> 2) ^ c) + (n & 3);
; #pragma unroll
;         for (int q = 0; q < 8; ++q) v[j][q] = s[32 * q] * wsc; }
;     if (t.f8) {
; #pragma unroll
;         for (int j = 0; j < 4; ++j) { const int n = (lane >> 3) + 8 * j;
;             int w0 = __builtin_amdgcn_cvt_pk_fp8_f32(v[j][0], v[j][1], 0, false); w0 = __builtin_amdgcn_cvt_pk_fp8_f32(v[j][2], v[j][3], w0, true);
;             int w1 = __builtin_amdgcn_cvt_pk_fp8_f32(v[j][4], v[j][5], 0, false); w1 = __builtin_amdgcn_cvt_pk_fp8_f32(v[j][6], v[j][7], w1, true);
;             u32x2 o; o.x = (unsigned)w0; o.y = (unsigned)w1;
;             __builtin_nontemporal_store(o, (u32x2*)((unsigned char*)t.WT + (size_t)(d0 + n) * t.K + k0 + 8 * c)); }
.Lg1c_catch:
	s_cmp_eq_u32 s32, 0
	s_cbranch_scc1 .Lg1c_c_loop
	s_waitcnt vmcnt(0)
	v_pk_mul_f32 v[16:17], v[16:17], s[94:95]
	v_pk_mul_f32 v[18:19], v[18:19], s[94:95]
	v_pk_mul_f32 v[20:21], v[20:21], s[94:95]
	v_pk_mul_f32 v[22:23], v[22:23], s[94:95]
	v_pk_mul_f32 v[24:25], v[24:25], s[94:95]
	v_pk_mul_f32 v[26:27], v[26:27], s[94:95]
	v_pk_mul_f32 v[28:29], v[28:29], s[94:95]
	v_pk_mul_f32 v[30:31], v[30:31], s[94:95]
	v_pk_mul_f32 v[32:33], v[32:33], s[94:95]
	v_pk_mul_f32 v[34:35], v[34:35], s[94:95]
	v_pk_mul_f32 v[36:37], v[36:37], s[94:95]
	v_pk_mul_f32 v[38:39], v[38:39], s[94:95]
	v_pk_mul_f32 v[40:41], v[40:41], s[94:95]
	v_pk_mul_f32 v[42:43], v[42:43], s[94:95]
	v_pk_mul_f32 v[44:45], v[44:45], s[94:95]
	v_pk_mul_f32 v[46:47], v[46:47], s[94:95]
	v_pk_mul_f32 v[48:49], v[48:49], s[94:95]
	v_pk_mul_f32 v[50:51], v[50:51], s[94:95]
	v_pk_mul_f32 v[52:53], v[52:53], s[94:95]
	v_pk_mul_f32 v[54:55], v[54:55], s[94:95]
	v_pk_mul_f32 v[56:57], v[56:57], s[94:95]
	v_pk_mul_f32 v[58:59], v[58:59], s[94:95]
	v_pk_mul_f32 v[60:61], v[60:61], s[94:95]
	v_pk_mul_f32 v[62:63], v[62:63], s[94:95]
	v_pk_mul_f32 v[208:209], v[208:209], s[94:95]
	v_pk_mul_f32 v[210:211], v[210:211], s[94:95]
	v_pk_mul_f32 v[212:213], v[212:213], s[94:95]
	v_pk_mul_f32 v[214:215], v[214:215], s[94:95]
	v_pk_mul_f32 v[244:245], v[244:245], s[94:95]
	v_pk_mul_f32 v[246:247], v[246:247], s[94:95]
	v_pk_mul_f32 v[248:249], v[248:249], s[94:95]
	v_pk_mul_f32 v[250:251], v[250:251], s[94:95]
	s_movk_i32 s99, 0x40
	v_lshlrev_b32_e32 v255, 4, v253
	v_cvt_pk_fp8_f32 v2, v16, v20
	v_cvt_pk_fp8_f32 v3, v32, v36
	v_cvt_pk_fp8_f32 v4, v48, v52
	v_cvt_pk_fp8_f32 v5, v208, v212
	v_cvt_pk_fp8_f32 v6, v17, v21
	v_cvt_pk_fp8_f32 v7, v33, v37
	v_cvt_pk_fp8_f32 v8, v49, v53
	v_cvt_pk_fp8_f32 v9, v209, v213
	v_cvt_pk_fp8_f32 v10, v18, v22
	v_cvt_pk_fp8_f32 v11, v34, v38
	v_cvt_pk_fp8_f32 v12, v50, v54
	v_cvt_pk_fp8_f32 v13, v210, v214
	v_cvt_pk_fp8_f32 v72, v19, v23
	v_cvt_pk_fp8_f32 v73, v35, v39
	v_cvt_pk_fp8_f32 v74, v51, v55
	v_cvt_pk_fp8_f32 v75, v211, v215
	v_mad_u32_u24 v255, v254, s99, v255
	v_add_u32_e32 v241, 0x100, v255
	v_cvt_pk_fp8_f32 v2, v24, v28 op_sel:[0,0,1]
	v_cvt_pk_fp8_f32 v3, v40, v44 op_sel:[0,0,1]
	v_cvt_pk_fp8_f32 v4, v56, v60 op_sel:[0,0,1]
	v_cvt_pk_fp8_f32 v5, v244, v248 op_sel:[0,0,1]
	v_cvt_pk_fp8_f32 v6, v25, v29 op_sel:[0,0,1]
	v_cvt_pk_fp8_f32 v7, v41, v45 op_sel:[0,0,1]
	v_cvt_pk_fp8_f32 v8, v57, v61 op_sel:[0,0,1]
	v_cvt_pk_fp8_f32 v9, v245, v249 op_sel:[0,0,1]
	v_cvt_pk_fp8_f32 v10, v26, v30 op_sel:[0,0,1]
	v_cvt_pk_fp8_f32 v11, v42, v46 op_sel:[0,0,1]
	v_cvt_pk_fp8_f32 v12, v58, v62 op_sel:[0,0,1]
	v_cvt_pk_fp8_f32 v13, v246, v250 op_sel:[0,0,1]
	v_cvt_pk_fp8_f32 v72, v27, v31 op_sel:[0,0,1]
	v_cvt_pk_fp8_f32 v73, v43, v47 op_sel:[0,0,1]
	v_cvt_pk_fp8_f32 v74, v59, v63 op_sel:[0,0,1]
	v_cvt_pk_fp8_f32 v75, v247, v251 op_sel:[0,0,1]
	global_store_dwordx4 v255, v[2:5], s[92:93] nt
	global_store_dwordx4 v241, v[6:9], s[92:93] nt
	v_add_u32_e32 v255, 0x200, v255
	v_add_u32_e32 v241, 0x200, v241
	global_store_dwordx4 v255, v[10:13], s[92:93] nt
	global_store_dwordx4 v241, v[72:75], s[92:93] nt
	s_mov_b32 s32, 0
.Lg1c_c_loop:
	s_cmp_lt_u32 s89, 16448
	s_cbranch_scc0 .Lg1c_c_done
	s_cmp_lt_u32 s89, 16448
	s_cbranch_scc0 .Lg1c_none_c
	s_lshr_b32 s98, s89, 6
	s_and_b32 s99, s89, 63
	s_cmp_lt_u32 s98, 256
	s_cselect_b32 s100, s98, 0
	s_cselect_b64 s[96:97], s[78:79], s[80:81]
	s_lshl_b32 s100, s100, 20
	s_lshr_b32 s101, s99, 5
	s_and_b32 s99, s99, 31
	s_lshl_b32 s77, s101, 19
	s_add_u32 s100, s100, s77
	s_lshl_b32 s77, s99, 7
	s_add_u32 s100, s100, s77
	s_add_u32 s96, s96, s100
	s_addc_u32 s97, s97, 0
	s_lshl_b32 s98, s98, 18
	s_lshl_b32 s77, s99, 13
	s_add_u32 s98, s98, s77
	s_lshl_b32 s77, s101, 7
	s_add_u32 s98, s98, s77
	s_add_u32 s92, s82, s98
	s_addc_u32 s93, s83, 0
	v_lshl_add_u32 v255, v253, 16, v254
	global_load_dwordx4 v[16:19], v255, s[96:97] nt
	s_add_u32 s96, s96, 0x1000
	s_addc_u32 s97, s97, 0
	global_load_dwordx4 v[20:23], v255, s[96:97] nt
	s_add_u32 s96, s96, 0x1000
	s_addc_u32 s97, s97, 0
	global_load_dwordx4 v[24:27], v255, s[96:97] nt
	s_add_u32 s96, s96, 0x1000
	s_addc_u32 s97, s97, 0
	global_load_dwordx4 v[28:31], v255, s[96:97] nt
	s_add_u32 s96, s96, 0x1000
	s_addc_u32 s97, s97, 0
	global_load_dwordx4 v[32:35], v255, s[96:97] nt
	s_add_u32 s96, s96, 0x1000
	s_addc_u32 s97, s97, 0
	global_load_dwordx4 v[36:39], v255, s[96:97] nt
	s_add_u32 s96, s96, 0x1000
	s_addc_u32 s97, s97, 0
	global_load_dwordx4 v[40:43], v255, s[96:97] nt
	s_add_u32 s96, s96, 0x1000
	s_addc_u32 s97, s97, 0
	global_load_dwordx4 v[44:47], v255, s[96:97] nt
	s_add_u32 s96, s96, 0x1000
	s_addc_u32 s97, s97, 0
	global_load_dwordx4 v[48:51], v255, s[96:97] nt
	s_add_u32 s96, s96, 0x1000
	s_addc_u32 s97, s97, 0
	global_load_dwordx4 v[52:55], v255, s[96:97] nt
	s_add_u32 s96, s96, 0x1000
	s_addc_u32 s97, s97, 0
	global_load_dwordx4 v[56:59], v255, s[96:97] nt
	s_add_u32 s96, s96, 0x1000
	s_addc_u32 s97, s97, 0
	global_load_dwordx4 v[60:63], v255, s[96:97] nt
	s_add_u32 s96, s96, 0x1000
	s_addc_u32 s97, s97, 0
	global_load_dwordx4 v[208:211], v255, s[96:97] nt
	s_add_u32 s96, s96, 0x1000
	s_addc_u32 s97, s97, 0
	global_load_dwordx4 v[212:215], v255, s[96:97] nt
	s_add_u32 s96, s96, 0x1000
	s_addc_u32 s97, s97, 0
	global_load_dwordx4 v[244:247], v255, s[96:97] nt
	s_add_u32 s96, s96, 0x1000
	s_addc_u32 s97, s97, 0
	global_load_dwordx4 v[248:251], v255, s[96:97] nt
	s_add_u32 s89, s89, s90
	s_mov_b32 s32, 1
; #define LAS __attribute__((address_space(3)))
; __device__ __forceinline__ void xcd_barrier(const XcdBarrier& b) {
;     asm volatile("s_waitcnt vmcnt(0)" ::: "memory");
;     __syncthreads();
;     if (threadIdx.x == 0) {
;         unsigned* bar = b.bar;
;         __builtin_amdgcn_s_waitcnt(0);
;         unsigned nloc = b.st[0], nx = b.st[1];
;         if (nloc == 0u) { xcd_barrier_complete(bar, b.x, nloc, nx); b.st[0] = nloc; b.st[1] = nx; }
; __device__ __forceinline__ void titem_finish(const TItem& t, int lane, const LAS unsigned char* buf) {
;     const int nblk = t.N / 32, kb = t.item / nblk, nb = t.item % nblk, k0 = 64 * kb, n0 = 32 * nb;
;     const int d0 = t.gmode == 0 ? n0 : ((n0 >> 7) * 256 + (n0 & 127) + (t.gmode == 2 ? 128 : 0));
;     const int c = lane & 7;
;     const LAS float* sb = (const LAS float*)buf;
;     float v[4][8];
;     const float wsc = t.scale;
; #pragma unroll
;     for (int j = 0; j < 4; ++j) { const int n = (lane >> 3) + 8 * j; const LAS float* s = sb + (8 * c) * 32 + 4 * ((n >> 2) ^ c) + (n & 3);
; #pragma unroll
;         for (int q = 0; q < 8; ++q) v[j][q] = s[32 * q] * wsc; }
;     if (t.f8) {
; #pragma unroll
;         for (int j = 0; j < 4; ++j) { const int n = (lane >> 3) + 8 * j;
;             int w0 = __builtin_amdgcn_cvt_pk_fp8_f32(v[j][0], v[j][1], 0, false); w0 = __builtin_amdgcn_cvt_pk_fp8_f32(v[j][2], v[j][3], w0, true);
;             int w1 = __builtin_amdgcn_cvt_pk_fp8_f32(v[j][4], v[j][5], 0, false); w1 = __builtin_amdgcn_cvt_pk_fp8_f32(v[j][6], v[j][7], w1, true);
;             u32x2 o; o.x = (unsigned)w0; o.y = (unsigned)w1;
;             __builtin_nontemporal_store(o, (u32x2*)((unsigned char*)t.WT + (size_t)(d0 + n) * t.K + k0 + 8 * c)); }
.Lg1c_none_c:
	s_waitcnt vmcnt(0)
	v_pk_mul_f32 v[16:17], v[16:17], s[94:95]
	v_pk_mul_f32 v[18:19], v[18:19], s[94:95]
	v_pk_mul_f32 v[20:21], v[20:21], s[94:95]
	v_pk_mul_f32 v[22:23], v[22:23], s[94:95]
	v_pk_mul_f32 v[24:25], v[24:25], s[94:95]
	v_pk_mul_f32 v[26:27], v[26:27], s[94:95]
	v_pk_mul_f32 v[28:29], v[28:29], s[94:95]
	v_pk_mul_f32 v[30:31], v[30:31], s[94:95]
	v_pk_mul_f32 v[32:33], v[32:33], s[94:95]
	v_pk_mul_f32 v[34:35], v[34:35], s[94:95]
	v_pk_mul_f32 v[36:37], v[36:37], s[94:95]
	v_pk_mul_f32 v[38:39], v[38:39], s[94:95]
	v_pk_mul_f32 v[40:41], v[40:41], s[94:95]
	v_pk_mul_f32 v[42:43], v[42:43], s[94:95]
	v_pk_mul_f32 v[44:45], v[44:45], s[94:95]
	v_pk_mul_f32 v[46:47], v[46:47], s[94:95]
	v_pk_mul_f32 v[48:49], v[48:49], s[94:95]
	v_pk_mul_f32 v[50:51], v[50:51], s[94:95]
	v_pk_mul_f32 v[52:53], v[52:53], s[94:95]
	v_pk_mul_f32 v[54:55], v[54:55], s[94:95]
	v_pk_mul_f32 v[56:57], v[56:57], s[94:95]
	v_pk_mul_f32 v[58:59], v[58:59], s[94:95]
	v_pk_mul_f32 v[60:61], v[60:61], s[94:95]
	v_pk_mul_f32 v[62:63], v[62:63], s[94:95]
	v_pk_mul_f32 v[208:209], v[208:209], s[94:95]
	v_pk_mul_f32 v[210:211], v[210:211], s[94:95]
	v_pk_mul_f32 v[212:213], v[212:213], s[94:95]
	v_pk_mul_f32 v[214:215], v[214:215], s[94:95]
	v_pk_mul_f32 v[244:245], v[244:245], s[94:95]
	v_pk_mul_f32 v[246:247], v[246:247], s[94:95]
	v_pk_mul_f32 v[248:249], v[248:249], s[94:95]
	v_pk_mul_f32 v[250:251], v[250:251], s[94:95]
	s_movk_i32 s99, 0x40
	v_lshlrev_b32_e32 v255, 4, v253
	v_cvt_pk_fp8_f32 v2, v16, v20
	v_cvt_pk_fp8_f32 v3, v32, v36
	v_cvt_pk_fp8_f32 v4, v48, v52
	v_cvt_pk_fp8_f32 v5, v208, v212
	v_cvt_pk_fp8_f32 v6, v17, v21
	v_cvt_pk_fp8_f32 v7, v33, v37
	v_cvt_pk_fp8_f32 v8, v49, v53
	v_cvt_pk_fp8_f32 v9, v209, v213
	v_cvt_pk_fp8_f32 v10, v18, v22
	v_cvt_pk_fp8_f32 v11, v34, v38
	v_cvt_pk_fp8_f32 v12, v50, v54
	v_cvt_pk_fp8_f32 v13, v210, v214
	v_cvt_pk_fp8_f32 v72, v19, v23
	v_cvt_pk_fp8_f32 v73, v35, v39
	v_cvt_pk_fp8_f32 v74, v51, v55
	v_cvt_pk_fp8_f32 v75, v211, v215
	v_mad_u32_u24 v255, v254, s99, v255
	v_add_u32_e32 v241, 0x100, v255
	v_cvt_pk_fp8_f32 v2, v24, v28 op_sel:[0,0,1]
	v_cvt_pk_fp8_f32 v3, v40, v44 op_sel:[0,0,1]
	v_cvt_pk_fp8_f32 v4, v56, v60 op_sel:[0,0,1]
	v_cvt_pk_fp8_f32 v5, v244, v248 op_sel:[0,0,1]
	v_cvt_pk_fp8_f32 v6, v25, v29 op_sel:[0,0,1]
	v_cvt_pk_fp8_f32 v7, v41, v45 op_sel:[0,0,1]
	v_cvt_pk_fp8_f32 v8, v57, v61 op_sel:[0,0,1]
	v_cvt_pk_fp8_f32 v9, v245, v249 op_sel:[0,0,1]
	v_cvt_pk_fp8_f32 v10, v26, v30 op_sel:[0,0,1]
	v_cvt_pk_fp8_f32 v11, v42, v46 op_sel:[0,0,1]
	v_cvt_pk_fp8_f32 v12, v58, v62 op_sel:[0,0,1]
	v_cvt_pk_fp8_f32 v13, v246, v250 op_sel:[0,0,1]
	v_cvt_pk_fp8_f32 v72, v27, v31 op_sel:[0,0,1]
	v_cvt_pk_fp8_f32 v73, v43, v47 op_sel:[0,0,1]
	v_cvt_pk_fp8_f32 v74, v59, v63 op_sel:[0,0,1]
	v_cvt_pk_fp8_f32 v75, v247, v251 op_sel:[0,0,1]
	global_store_dwordx4 v255, v[2:5], s[92:93] nt
	global_store_dwordx4 v241, v[6:9], s[92:93] nt
	v_add_u32_e32 v255, 0x200, v255
	v_add_u32_e32 v241, 0x200, v241
	global_store_dwordx4 v255, v[10:13], s[92:93] nt
	global_store_dwordx4 v241, v[72:75], s[92:93] nt
	s_nop 1
	s_mov_b32 s32, 0
	s_branch .Lg1c_c_loop
.Lg1c_c_done:
.LBB0_761:
	s_add_u32 s66, s60, 0x200
	s_addc_u32 s67, s61, 0
	s_add_u32 s76, s60, 0x1000
	s_addc_u32 s77, s61, 0
	s_add_u32 s78, s60, 0x1100
	s_addc_u32 s79, s61, 0
	s_add_u32 s80, s60, 0x1200
	s_addc_u32 s81, s61, 0
	s_add_u32 s82, s60, 0x1300
	s_addc_u32 s83, s61, 0
	s_cmp_eq_u32 s57, 15
	s_cselect_b64 s[4:5], -1, 0
	s_cmp_eq_u32 s57, 14
	v_writelane_b32 v252, s4, 0
	s_waitcnt lgkmcnt(0)
	v_cmp_eq_u32_e64 s[20:21], 0, v0
	v_writelane_b32 v252, s5, 1
	s_cselect_b64 s[4:5], -1, 0
	v_writelane_b32 v252, s4, 2
	s_cmp_eq_u32 s57, 13
	s_nop 0
	v_writelane_b32 v252, s5, 3
	s_cselect_b64 s[4:5], -1, 0
	v_writelane_b32 v252, s4, 4
	s_cmp_eq_u32 s57, 12
	s_nop 0
	v_writelane_b32 v252, s5, 5
	s_cselect_b64 s[4:5], -1, 0
	v_writelane_b32 v252, s4, 6
	s_cmp_eq_u32 s57, 11
	s_nop 0
	v_writelane_b32 v252, s5, 7
	s_cselect_b64 s[4:5], -1, 0
	v_writelane_b32 v252, s4, 8
	s_cmp_eq_u32 s57, 10
	s_nop 0
	v_writelane_b32 v252, s5, 9
	s_cselect_b64 s[4:5], -1, 0
	v_writelane_b32 v252, s4, 10
	s_cmp_eq_u32 s57, 9
	s_nop 0
	v_writelane_b32 v252, s5, 11
	s_cselect_b64 s[4:5], -1, 0
	v_writelane_b32 v252, s4, 12
	s_cmp_eq_u32 s57, 8
	s_nop 0
	v_writelane_b32 v252, s5, 13
	s_cselect_b64 s[4:5], -1, 0
	v_writelane_b32 v252, s4, 14
	s_cmp_eq_u32 s57, 7
	s_nop 0
	v_writelane_b32 v252, s5, 15
	s_cselect_b64 s[4:5], -1, 0
	v_writelane_b32 v252, s4, 16
	s_cmp_eq_u32 s57, 6
	s_nop 0
	v_writelane_b32 v252, s5, 17
	s_cselect_b64 s[4:5], -1, 0
	v_writelane_b32 v252, s4, 18
	s_cmp_eq_u32 s57, 5
	s_nop 0
	v_writelane_b32 v252, s5, 19
	s_cselect_b64 s[4:5], -1, 0
	v_writelane_b32 v252, s4, 20
	s_cmp_eq_u32 s57, 4
	s_nop 0
	v_writelane_b32 v252, s5, 21
	s_cselect_b64 s[4:5], -1, 0
	v_writelane_b32 v252, s4, 22
	s_cmp_eq_u32 s57, 3
	s_nop 0
	v_writelane_b32 v252, s5, 23
	s_cselect_b64 s[4:5], -1, 0
	v_writelane_b32 v252, s4, 24
	s_cmp_eq_u32 s57, 2
	s_nop 0
	v_writelane_b32 v252, s5, 25
	s_cselect_b64 s[4:5], -1, 0
	v_writelane_b32 v252, s4, 26
	s_cmp_eq_u32 s57, 1
	s_nop 0
	v_writelane_b32 v252, s5, 27
	s_cselect_b64 s[4:5], -1, 0
	v_writelane_b32 v252, s4, 28
	s_cmp_eq_u32 s57, 0
	s_nop 0
	v_writelane_b32 v252, s5, 29
	s_cselect_b64 s[4:5], -1, 0
	v_writelane_b32 v252, s4, 30
	s_nop 1
	v_writelane_b32 v252, s5, 31
	s_lshl_b32 s4, s57, 8
	s_add_u32 s4, s60, s4
	s_addc_u32 s5, s61, 0
	s_add_u32 s74, s4, 0x1400
	s_addc_u32 s75, s5, 0
	s_add_u32 s68, s4, 0x2400
	s_addc_u32 s69, s5, 0
	s_add_u32 s72, s60, 0x3400
	s_addc_u32 s73, s61, 0
	s_add_u32 s70, s60, 0x3500
	s_addc_u32 s71, s61, 0
	s_cmp_gt_i32 s63, 10
	s_cselect_b64 s[40:41], -1, 0
	s_and_b64 s[4:5], s[38:39], s[40:41]
	s_andn2_b64 vcc, exec, s[4:5]
	s_cbranch_vccnz .LBB0_820
	s_waitcnt vmcnt(0)
	s_waitcnt vmcnt(0)
	s_barrier
	s_and_saveexec_b64 s[42:43], s[20:21]
	s_cbranch_execz .LBB0_819
	v_mov_b32_e32 v1, s91
	s_waitcnt vmcnt(0) expcnt(0) lgkmcnt(0)
	ds_read_b32 v3, v1
	ds_read_b32 v1, v1 offset:4
	s_waitcnt lgkmcnt(1)
	v_cmp_ne_u32_e32 vcc, 0, v3
	s_cbranch_vccnz .LBB0_787
	s_load_dwordx2 s[4:5], s[64:65], 0x0
	s_load_dword s7, s[64:65], 0x8
	s_mov_b32 s6, 1
	v_mov_b32_e32 v17, 0
	s_waitcnt lgkmcnt(0)
	s_mul_i32 s4, s5, s4
	s_mul_i32 s7, s4, s7
	s_branch .LBB0_766
